# baseline (speedup 1.0000x reference)
.LBB0_9:
	s_or_b64 exec, exec, s[6:7]
	s_movk_i32 s3, 0x188
	v_cmp_gt_u32_e32 vcc, s3, v0
	s_and_saveexec_b64 s[6:7], vcc
	v_mov_b32_e32 v14, 0
	ds_write_b32 v10, v14 offset:32000
	s_or_b64 exec, exec, s[6:7]
	s_waitcnt vmcnt(3)
	v_cmp_lt_i32_e64 s[18:19], -1, v34
	v_mov_b32_e32 v17, 0
	v_lshrrev_b32_e32 v44, 5, v34
	v_mov_b32_e32 v43, 0
	s_waitcnt lgkmcnt(0)
	s_barrier
	s_and_saveexec_b64 s[6:7], s[18:19]
	v_and_b32_e32 v14, 0x7fffffc, v44
	v_mov_b32_e32 v15, 1
	ds_add_rtn_u32 v43, v14, v15 offset:32000
	s_or_b64 exec, exec, s[6:7]
	s_waitcnt vmcnt(2)
	v_cmp_lt_i32_e64 s[16:17], -1, v32
	v_lshrrev_b32_e32 v42, 5, v32
	s_and_saveexec_b64 s[6:7], s[16:17]
	v_and_b32_e32 v14, 0x7fffffc, v42
	v_mov_b32_e32 v15, 1
	ds_add_rtn_u32 v17, v14, v15 offset:32000
	s_or_b64 exec, exec, s[6:7]
	v_cmp_lt_i32_e64 s[14:15], -1, v30
	v_mov_b32_e32 v16, 0
	v_lshrrev_b32_e32 v41, 5, v30
	v_mov_b32_e32 v40, 0
	s_and_saveexec_b64 s[6:7], s[14:15]
	v_and_b32_e32 v14, 0x7fffffc, v41
	v_mov_b32_e32 v15, 1
	ds_add_rtn_u32 v40, v14, v15 offset:32000
	s_or_b64 exec, exec, s[6:7]
	s_waitcnt vmcnt(1)
	v_cmp_lt_i32_e64 s[12:13], -1, v31
	v_lshrrev_b32_e32 v39, 5, v31
	s_and_saveexec_b64 s[6:7], s[12:13]
	v_and_b32_e32 v14, 0x7fffffc, v39
	v_mov_b32_e32 v15, 1
	ds_add_rtn_u32 v16, v14, v15 offset:32000
	s_or_b64 exec, exec, s[6:7]
	v_cmp_lt_i32_e64 s[10:11], -1, v27
	v_mov_b32_e32 v15, 0
	v_lshrrev_b32_e32 v38, 5, v27
	v_mov_b32_e32 v37, 0
	s_and_saveexec_b64 s[6:7], s[10:11]
	v_and_b32_e32 v14, 0x7fffffc, v38
	v_mov_b32_e32 v18, 1
	ds_add_rtn_u32 v37, v14, v18 offset:32000
	s_or_b64 exec, exec, s[6:7]
	s_waitcnt vmcnt(0)
	v_cmp_lt_i32_e64 s[8:9], -1, v26
	v_lshrrev_b32_e32 v36, 5, v26
	s_and_saveexec_b64 s[6:7], s[8:9]
	v_and_b32_e32 v14, 0x7fffffc, v36
	v_mov_b32_e32 v15, 1
	ds_add_rtn_u32 v15, v14, v15 offset:32000
	s_or_b64 exec, exec, s[6:7]
	v_cmp_lt_i32_e64 s[6:7], -1, v24
	v_mov_b32_e32 v14, 0
	v_lshrrev_b32_e32 v35, 5, v24
	v_mov_b32_e32 v19, 0
	s_and_saveexec_b64 s[20:21], s[6:7]
	v_and_b32_e32 v18, 0x7fffffc, v35
	v_mov_b32_e32 v19, 1
	ds_add_rtn_u32 v19, v18, v19 offset:32000
	s_or_b64 exec, exec, s[20:21]
	v_cmp_lt_i32_e32 vcc, -1, v21
	v_lshrrev_b32_e32 v18, 5, v21
	s_and_saveexec_b64 s[20:21], vcc
	v_and_b32_e32 v14, 0x7fffffc, v18
	v_mov_b32_e32 v45, 1
	ds_add_rtn_u32 v14, v14, v45 offset:32000
	s_or_b64 exec, exec, s[20:21]
	s_movk_i32 s3, 0x187
	v_cmp_gt_u32_e64 s[20:21], s3, v0
	v_mov_b32_e32 v45, 0
	s_waitcnt lgkmcnt(0)
	s_barrier
	s_and_saveexec_b64 s[24:25], s[20:21]
	ds_read_b32 v45, v10 offset:32000
	s_or_b64 exec, exec, s[24:25]
	v_and_b32_e32 v49, 63, v0
	v_lshrrev_b32_e32 v47, 6, v0
	s_waitcnt lgkmcnt(0)
	v_mov_b32_e32 v46, v45
	s_nop 4
	v_add_u32_dpp v46, v46, v46 row_shr:1 row_mask:0xf bank_mask:0xf bound_ctrl:0
	s_nop 1
	v_add_u32_dpp v46, v46, v46 row_shr:2 row_mask:0xf bank_mask:0xf bound_ctrl:0
	s_nop 1
	v_add_u32_dpp v46, v46, v46 row_shr:4 row_mask:0xf bank_mask:0xf bound_ctrl:0
	s_nop 1
	v_add_u32_dpp v46, v46, v46 row_shr:8 row_mask:0xf bank_mask:0xf bound_ctrl:0
	s_nop 1
	v_add_u32_dpp v46, v46, v46 row_bcast:15 row_mask:0xa bank_mask:0xf
	s_nop 1
	v_add_u32_dpp v46, v46, v46 row_bcast:31 row_mask:0xc bank_mask:0xf
	s_nop 1
	v_cmp_eq_u32_e64 s[24:25], 63, v49
	s_and_saveexec_b64 s[28:29], s[24:25]
	v_lshlrev_b32_e32 v48, 2, v47
	ds_write_b32 v48, v46 offset:35136
	s_or_b64 exec, exec, s[28:29]
	s_load_dwordx4 s[28:31], s[0:1], 0x28
	v_cmp_lt_u32_e64 s[24:25], 63, v0
	v_mov_b32_e32 v48, 0
	s_waitcnt lgkmcnt(0)
	s_barrier
	v_mov_b32_e32 v49, 0x8940
	ds_read_b128 v[50:53], v49
	ds_read_b128 v[54:57], v49 offset:16
	v_cmp_lt_u32_e64 s[24:25], 0, v47
	v_cmp_lt_u32_e64 s[34:35], 1, v47
	v_cmp_lt_u32_e64 s[36:37], 2, v47
	v_cmp_lt_u32_e64 s[38:39], 3, v47
	s_waitcnt lgkmcnt(0)
	v_cndmask_b32_e64 v48, 0, v50, s[24:25]
	v_cndmask_b32_e64 v50, 0, v51, s[34:35]
	v_cndmask_b32_e64 v51, 0, v52, s[36:37]
	v_cndmask_b32_e64 v52, 0, v53, s[38:39]
	v_cmp_lt_u32_e64 s[24:25], 4, v47
	v_cmp_lt_u32_e64 s[34:35], 5, v47
	v_cmp_lt_u32_e64 s[36:37], 6, v47
	v_add_u32_e32 v48, v48, v50
	v_add3_u32 v48, v48, v51, v52
	v_cndmask_b32_e64 v50, 0, v54, s[24:25]
	v_cndmask_b32_e64 v51, 0, v55, s[34:35]
	v_cndmask_b32_e64 v52, 0, v56, s[36:37]
	v_add_u32_e32 v48, v48, v50
	v_add3_u32 v48, v48, v51, v52
	s_and_saveexec_b64 s[24:25], s[20:21]
	s_cbranch_execz .LBB0_43
	v_sub_u32_e32 v46, v46, v45
	v_add_u32_e32 v46, v46, v48
	ds_write_b32 v10, v46 offset:33568
	v_lshl_or_b32 v10, v45, 16, v46
	s_movk_i32 s3, 0xc8
	v_mov_b32_e32 v45, s2
	v_mad_u32_u24 v46, v0, s3, v45
	v_mov_b32_e32 v47, 0
	v_lshl_add_u64 v[46:47], v[46:47], 2, s[28:29]
	global_store_dword v[46:47], v10, off sc1
